# speedup vs baseline: 1.0001x; 1.0001x over previous
.LBB3_11:
	s_lshl_b32 s58, s42, 7
	s_add_i32 s59, s41, 0x400
	s_lshr_b32 s59, s59, 6
	s_bfe_u32 s60, s20, 0x1000c
	s_add_i32 s59, s59, s60
	s_lshl_b32 s59, s59, 19
	s_add_u32 s58, s58, s59
	s_add_u32 s58, s56, s58
	s_addc_u32 s59, s57, 0
	s_add_u32 s60, s58, 0x4000
	s_addc_u32 s61, s59, 0
	s_add_u32 s62, s58, 0x100000
	s_addc_u32 s63, s59, 0
	s_add_u32 s64, s62, 0x4000
	s_addc_u32 s65, s63, 0
	s_lshr_b32 s66, s41, 7
	s_bfe_u32 s67, s20, 0x1000c
	s_add_i32 s66, s66, s67
	s_lshl_b32 s66, s66, 14
	s_lshl_b32 s67, s42, 2
	s_add_u32 s66, s66, s67
	s_add_u32 s66, s14, s66
	s_addc_u32 s67, s15, 0
	v_add_u32_e32 v172, s43, v207
	v_pk_fma_f32 v[244:245], v[244:245], -0.5, -0.5 op_sel_hi:[1,0,0]
	v_pk_fma_f32 v[246:247], v[246:247], -0.5, -0.5 op_sel_hi:[1,0,0]
	v_pk_fma_f32 v[248:249], v[248:249], -0.5, -0.5 op_sel_hi:[1,0,0]
	v_pk_fma_f32 v[250:251], v[250:251], -0.5, -0.5 op_sel_hi:[1,0,0]
	v_pk_fma_f32 v[252:253], v[252:253], -0.5, -0.5 op_sel_hi:[1,0,0]
	v_pk_fma_f32 v[254:255], v[254:255], -0.5, -0.5 op_sel_hi:[1,0,0]
	v_pk_fma_f32 v[232:233], v[232:233], -0.5, -0.5 op_sel_hi:[1,0,0]
	v_pk_fma_f32 v[234:235], v[234:235], -0.5, -0.5 op_sel_hi:[1,0,0]
	v_pk_mul_f32 v[134:135], v[244:245], v[246:247]
	v_pk_mul_f32 v[146:147], v[248:249], v[250:251]
	v_pk_mul_f32 v[180:181], v[252:253], v[254:255]
	v_pk_mul_f32 v[236:237], v[232:233], v[234:235]
	v_mul_f32_e32 v188, v134, v135
	v_mul_f32_e32 v190, v146, v147
	v_mul_f32_e32 v189, v180, v181
	v_mul_f32_e32 v191, v236, v237
	v_pk_mul_f32 v[192:193], v[188:189], v[190:191]
	v_mul_f32_e32 v162, v192, v193
	v_rcp_f32_e32 v173, v162
	v_pk_add_f32 v[164:165], v[114:115], v[116:117]
	v_pk_add_f32 v[164:165], v[164:165], v[78:79]
	v_pk_add_f32 v[164:165], v[164:165], v[80:81]
	v_pk_add_f32 v[164:165], v[164:165], v[106:107]
	v_pk_add_f32 v[164:165], v[164:165], v[108:109]
	v_pk_add_f32 v[164:165], v[164:165], v[70:71]
	v_pk_add_f32 v[164:165], v[164:165], v[72:73]
	v_pk_mul_f32 v[230:231], v[172:173], v[192:193] op_sel:[1,1] op_sel_hi:[1,0]
	v_pk_mul_f32 v[192:193], v[230:231], v[190:191]
	v_pk_mul_f32 v[190:191], v[230:231], v[188:189]
	v_pk_mul_f32 v[136:137], v[192:193], v[134:135] op_sel:[0,1] op_sel_hi:[0,0]
	v_pk_mul_f32 v[148:149], v[190:191], v[146:147] op_sel:[0,1] op_sel_hi:[0,0]
	v_pk_mul_f32 v[182:183], v[192:193], v[180:181] op_sel:[1,1] op_sel_hi:[1,0]
	v_pk_mul_f32 v[238:239], v[190:191], v[236:237] op_sel:[1,1] op_sel_hi:[1,0]
	v_pk_fma_f32 v[138:139], v[136:137], v[246:247], 1.0 op_sel_hi:[1,1,0]
	v_pk_fma_f32 v[140:141], v[136:137], v[244:245], 1.0 op_sel_hi:[1,1,0]
	v_pk_fma_f32 v[150:151], v[148:149], v[250:251], 1.0 op_sel_hi:[1,1,0]
	v_pk_fma_f32 v[152:153], v[148:149], v[248:249], 1.0 op_sel_hi:[1,1,0]
	v_pk_fma_f32 v[184:185], v[182:183], v[254:255], 1.0 op_sel_hi:[1,1,0]
	v_pk_fma_f32 v[186:187], v[182:183], v[252:253], 1.0 op_sel_hi:[1,1,0]
	v_pk_fma_f32 v[240:241], v[238:239], v[234:235], 1.0 op_sel_hi:[1,1,0]
	v_pk_fma_f32 v[242:243], v[238:239], v[232:233], 1.0 op_sel_hi:[1,1,0]
	v_cvt_pk_bf16_f32 v154, v138, v139
	v_cvt_pk_bf16_f32 v155, v140, v141
	v_cvt_pk_bf16_f32 v156, v150, v151
	v_cvt_pk_bf16_f32 v157, v152, v153
	v_cvt_pk_bf16_f32 v158, v184, v185
	v_cvt_pk_bf16_f32 v159, v186, v187
	v_cvt_pk_bf16_f32 v160, v240, v241
	v_cvt_pk_bf16_f32 v161, v242, v243
	ds_read_b128 v[114:117], v172
	ds_read_b128 v[78:81], v172 offset:64
	ds_read_b128 v[106:109], v172 offset:128
	ds_read_b128 v[70:73], v172 offset:192
	v_permlane16_swap_b32_e32 v154, v156
	v_permlane16_swap_b32_e32 v155, v157
	global_store_dwordx4 v228, v[154:157], s[58:59] nt
	s_bitcmp1_b32 s20, 12
	s_cbranch_scc1 .Lg1_noX
	s_barrier
	s_branch .Lg1_aftX
.Lg1_noX:
	s_setprio 1
